# v67 with a larger layer-1 chunk converted inside layer 1's in-projection phase (4880 items) and layer 0's split rebalanced to 5184/304 (all boundaries multiples of 8)
# baseline (speedup 1.0000x reference)
; #define LAS __attribute__((address_space(3)))
; __device__ __forceinline__ int opaque_tid() { int t = threadIdx.x; asm volatile("" : "+v"(t)); return t; }
;     __device__ __forceinline__ bool next(int i, Unit& u) const {
;         const long L = (long)i * G + c; if (L >= nwg) return false;
;         int wgid = (int)L; { const int q = nwg / NXCD, r = nwg % NXCD, xcd = wgid % NXCD, off = wgid / NXCD; wgid = (xcd < r ? xcd * (q + 1) : r * (q + 1) + (xcd - r) * q) + off; }
;         const int nig = WGM * nN, gid = wgid / nig, fm = gid * WGM, gsz = (nM - fm) < WGM ? (nM - fm) : WGM;
;         u.pm = fm + ((wgid % nig) % gsz); u.pn = (wgid % nig) / gsz; u.e = 0; u.rows = 256;
;         u.a = A + (size_t)u.pm * tstepA; u.b = Bt + (size_t)u.pn * tstep; return true;
; __device__ __forceinline__ void pj_mfma(const Args& a, LAS unsigned char* lds, int layer) {
;     pg8::DenseOrder So; So.init(a.ws + WS_ACT, a.ws + WS_WIN + (size_t)layer * 3328 * D * 2, NTOK, 3328, D, gridDim.x, blockIdx.x);
;     LAS float* gl = (LAS float*)(lds + SEG_OFF + 256);
;     { const int t_ = opaque_tid(); if (t_ < 256) { const int w = t_ >> 6, i = t_ & 63; const float* gp_ = w == 0 ? a.in[I_QGF] : w == 1 ? a.in[I_KGF] : w == 2 ? a.in[I_QGD] : a.in[I_KGD]; gl[t_] = gp_[layer * 64 + i]; } }
;     __syncthreads();
;     EpiProj E{(bf16_t*)(a.ws + WS_PROJ), gl};
;     pg8::gemm_phase<EpiProj, pg8::DenseOrder>(lds, D, So, E);
;     if ((int)blockIdx.x >= (int)gridDim.x - 32) cumsum_unit(a, lds, blockIdx.x - (gridDim.x - 32));
;     if (layer + 1 < NL) { __syncthreads(); constexpr int I_SPLIT = 10240;
;         const int half = gridDim.x / 2; const bool upper = (int)blockIdx.x >= half;
;         p0_prep(a, lds, layer + 1, upper ? half : 0, upper ? (int)gridDim.x - half : half, upper ? 0 : I_SPLIT, upper ? I_SPLIT : (1 << 30)); }
.LBB0_101:
	s_or_b64 exec, exec, s[0:1]
	s_mov_b32 vcc_lo, 0
	s_nop 1
	v_writelane_b32 v254, vcc_lo, 60
	s_nop 1
	s_mov_b32 vcc_lo, 0
	s_nop 1
	v_writelane_b32 v254, vcc_lo, 62
	s_nop 1
	s_waitcnt lgkmcnt(0)
	s_barrier
	s_load_dwordx2 s[92:93], s[54:55], 0xa0
	s_load_dwordx16 s[12:27], s[54:55], 0x20
	s_load_dwordx4 s[0:3], s[54:55], 0x90
	s_movk_i32 s5, 0xd1
	s_mov_b32 s67, 0
	s_waitcnt vmcnt(0)
	v_mbcnt_lo_u32_b32 v1, -1, 0
	v_mbcnt_hi_u32_b32 v199, -1, v1
	s_waitcnt lgkmcnt(0)
	v_writelane_b32 v252, s0, 8
	v_and_b32_e32 v240, 64, v199
	s_mul_hi_u32 s85, s77, 0x600
	v_writelane_b32 v252, s1, 9
	v_writelane_b32 v252, s2, 10
	v_writelane_b32 v252, s3, 11
	s_add_u32 s0, s92, 0x100000
	s_addc_u32 s1, s93, 0
	v_writelane_b32 v252, s0, 12
	s_add_u32 s96, s92, 0xbc00000
	s_addc_u32 s97, s93, 0
	v_writelane_b32 v252, s1, 13
	s_lshl_b32 s0, s61, 3
	s_add_u32 s10, s92, 0x180000
	s_addc_u32 s11, s93, 0
	s_add_u32 s80, s92, 0x7c00000
	s_addc_u32 s81, s93, 0
	v_writelane_b32 v252, s0, 14
	s_add_u32 s0, s92, 0xfc00000
	s_addc_u32 s1, s93, 0
	s_add_u32 s50, s92, 0x18c00000
	s_addc_u32 s51, s93, 0
	s_add_u32 s2, s92, 0xa00000
	s_addc_u32 s3, s93, 0
	v_writelane_b32 v252, s2, 15
	s_cmpk_lt_i32 s61, 0x680
	s_mul_i32 s84, s77, 0x600
	v_writelane_b32 v252, s3, 16
	s_cselect_b64 s[2:3], -1, 0
	v_writelane_b32 v252, s2, 17
	v_mov_b32_e32 v35, 0
	v_add_u32_e32 v241, 64, v240
	v_writelane_b32 v252, s3, 18
	s_ashr_i32 s2, s61, 31
	v_writelane_b32 v252, s2, 19
	s_lshr_b32 s2, s2, 29
	s_add_i32 s3, s61, s2
	s_ashr_i32 s2, s3, 3
	s_and_b32 s3, s3, -8
	s_sub_i32 s3, s61, s3
	s_lshl_b32 s4, s3, 6
	s_cmp_lt_i32 s3, 0
	s_cselect_b32 s5, s5, 0xd0
	s_mul_i32 s5, s5, s3
	s_mulk_i32 s3, 0x41
	s_cselect_b32 s3, s3, s4
	s_add_i32 s5, s5, s2
	s_mul_hi_i32 s4, s5, 0x4ec4ec4f
	s_lshr_b32 s6, s4, 31
	s_ashr_i32 s4, s4, 5
	s_add_i32 s4, s4, s6
	s_mul_i32 s6, s4, 0x68
	s_sub_i32 s5, s5, s6
	s_lshl_b32 s7, s4, 3
	s_bfe_i32 s4, s5, 0x80000
	s_bfe_u32 s4, s4, 0x3000c
	s_add_i32 s6, s5, s4
	s_bfe_i32 s4, s6, 0x80000
	s_and_b32 s6, s6, 0xf8
	s_sub_i32 s5, s5, s6
	s_sext_i32_i16 s8, s4
	s_sext_i32_i8 s5, s5
	s_add_i32 s28, s7, s5
	s_ashr_i32 s5, s8, 3
	v_writelane_b32 v252, s5, 20
	s_mov_b32 s6, s28
	s_ashr_i32 s29, s28, 31
	v_writelane_b32 v252, s6, 21
	s_lshr_b32 s4, s8, 3
	v_xor_b32_e32 v236, 16, v199
	v_writelane_b32 v252, s7, 22
	s_lshl_b64 s[6:7], s[28:29], 19
	s_add_u32 s6, s80, s6
	s_addc_u32 s7, s81, s7
	v_writelane_b32 v252, s6, 23
	s_bfe_i64 s[4:5], s[4:5], 0x100000
	s_lshl_b64 s[4:5], s[4:5], 19
	v_writelane_b32 v252, s7, 24
	v_writelane_b32 v252, s4, 25
	v_xor_b32_e32 v237, 32, v199
	v_mov_b32_e32 v238, 1
	v_writelane_b32 v252, s5, 26
	s_ashr_i32 s4, s77, 31
	v_writelane_b32 v252, s4, 27
	s_sub_i32 s4, s77, 32
	s_cmp_ge_i32 s61, s4
	s_cselect_b64 s[6:7], -1, 0
	v_writelane_b32 v252, s6, 28
	s_sub_i32 s4, s61, s4
	s_and_b32 s5, s4, 3
	v_writelane_b32 v252, s7, 29
	s_ashr_i32 s6, s4, 2
	s_ashr_i32 s7, s6, 31
	s_lshl_b32 s5, s5, 2
	s_add_u32 s5, s10, s5
	v_writelane_b32 v252, s10, 30
	s_addc_u32 s8, s11, 0
	s_lshl_b64 s[6:7], s[6:7], 16
	s_add_u32 s6, s5, s6
	s_addc_u32 s7, s8, s7
	s_add_u32 s28, s92, 0x200000
	s_addc_u32 s29, s93, 0
	s_ashr_i32 s5, s4, 31
	s_lshl_b64 s[4:5], s[4:5], 14
	v_writelane_b32 v252, s11, 31
	s_add_u32 s4, s28, s4
	v_writelane_b32 v252, s6, 32
	s_addc_u32 s5, s29, s5
	s_lshr_b32 s8, s77, 1
	v_writelane_b32 v252, s7, 33
	s_sub_i32 s9, s77, s8
	v_writelane_b32 v252, s4, 34
	s_cmp_lt_i32 s61, s8
	v_mov_b32_e32 v198, 0x358637bd
	v_writelane_b32 v252, s5, 35
	s_cselect_b64 s[4:5], -1, 0
	s_and_b64 s[6:7], s[4:5], exec
	s_cselect_b32 s6, s8, s9
	s_movk_i32 s7, 0x1570
	s_cselect_b32 s10, 0, s8
	s_cselect_b32 s8, 0x1440, 0
	s_cselect_b32 s7, s7, 0x1440
	s_lshl_b32 s6, s6, 3
	v_writelane_b32 v252, s7, 36
	s_cmp_ge_i32 s61, s10
	v_writelane_b32 v252, s6, 37
	s_cselect_b64 s[6:7], -1, 0
	s_or_b64 s[4:5], s[36:37], s[4:5]
	s_load_dwordx8 s[36:43], s[54:55], 0x60
	s_and_b64 s[4:5], s[6:7], s[4:5]
	v_writelane_b32 v252, s4, 38
	v_mov_b32_e32 v201, 1.0
	v_mov_b32_e32 v239, 0x7f800000
	v_writelane_b32 v252, s5, 39
	s_sub_i32 s4, s61, s10
	s_lshl_b32 s4, s4, 3
	s_add_i32 s4, s4, s8
	s_waitcnt lgkmcnt(0)
	s_mov_b64 s[8:9], s[40:41]
	v_writelane_b32 v252, s4, 40
	s_add_u32 s6, s38, 0x400000
	s_mov_b64 s[10:11], s[42:43]
	s_mov_b64 s[4:5], s[36:37]
	v_writelane_b32 v252, s4, 41
	v_mov_b32_e32 v202, 0x3f317218
	v_mov_b32_e32 v242, 0xff800000
	v_writelane_b32 v252, s5, 42
	v_writelane_b32 v252, s6, 43
	v_writelane_b32 v252, s7, 44
	v_writelane_b32 v252, s8, 45
	v_writelane_b32 v252, s9, 46
	v_writelane_b32 v252, s10, 47
	v_writelane_b32 v252, s11, 48
	s_addc_u32 s7, s39, 0
	v_writelane_b32 v252, s6, 49
	s_add_u32 s4, s16, 0xd04000
	s_movk_i32 s74, 0x1ff
	v_writelane_b32 v252, s7, 50
	v_writelane_b32 v252, s12, 51
	s_addc_u32 s5, s17, 0
	s_mov_b32 s76, 0x800000
	v_writelane_b32 v255, s25, 0
	v_writelane_b32 v255, s26, 1
	v_writelane_b32 v255, s27, 2
	v_writelane_b32 v255, s4, 3
	v_writelane_b32 v252, s13, 52
	v_writelane_b32 v252, s14, 53
	v_writelane_b32 v255, s5, 4
	s_add_u32 s4, s92, 0x5b00000
	s_addc_u32 s5, s93, 0
	v_writelane_b32 v255, s4, 5
	v_writelane_b32 v252, s15, 54
	v_writelane_b32 v252, s16, 55
	v_writelane_b32 v255, s5, 6
	s_add_u32 s4, s92, 0x1b00000
	s_addc_u32 s5, s93, 0
	s_add_u32 s82, s92, 0x700000
	v_writelane_b32 v255, s4, 7
	s_addc_u32 s83, s93, 0
	v_writelane_b32 v252, s17, 56
	v_writelane_b32 v255, s5, 8
	s_add_u32 s4, s92, 0x14000
	v_writelane_b32 v255, s4, 9
	s_addc_u32 s4, s93, 0
	s_add_i32 s6, s61, 0x900
	s_cmpk_lt_i32 s61, 0x200
	v_writelane_b32 v255, s4, 10
	s_cselect_b64 s[4:5], -1, 0
	v_writelane_b32 v255, s4, 11
	v_writelane_b32 v252, s18, 57
;     ...
;         if (u < AT_NFOX) {
;             const int qb = 15 - (u >> 5), bh = u & 31, b = bh >> 2, h = bh & 3, q0 = qb * 256;
;             const size_t rb = (size_t)b * S;
;             const bf16_t* Kb = proj + ((size_t)(4 + h) * NTOK + rb) * 64;
;             const bf16_t* Vb = proj + ((size_t)(8 + h) * NTOK + rb) * 64;
;             const float* cum = cumall + (size_t)bh * S;
;             const int jhi = 4 * qb + 3;
;             fox_cr = cum[q0]; fox_cv = cum[64 * (lane <= jhi ? lane : jhi) + 63]; fox_cq = cum[q0 + 32 * wid + r32];
;             if (!(dbg & 1)) { FOX_ISSUE(0); FOX_ISSUE(1); FOX_ISSUE(2); }
;             const bf16_t* Q = proj + ((size_t)(0 + h) * NTOK + rb + q0 + 32 * wid + r32) * 64;
; #pragma unroll
;             for (int d0 = 0; d0 < 4; ++d0) qr[d0] = *(const bf16x8*)(Q + d0 * 16 + hi * 8);
;         } else if (u < AT_NFOX + AT_NDIL) {
;             const int v2 = u - AT_NFOX, bh = v2 % 48, rest = v2 / 48, b = bh / 6, h = bh % 6, p = rest >> 4, x = rest & 15;
;             const int dil = p == 0 ? 1 : p == 1 ? 4 : 16, res = x % dil, nb2 = x / dil;
;             const size_t rb = (size_t)b * S;
;             const bf16_t* Kb = proj + ((size_t)(22 + h) * NTOK + rb) * 64;
;             const bf16_t* Vb = proj + ((size_t)(28 + h) * NTOK + rb) * 64;
;             const int mk_base = 256 * nb2 - 128, tt_lo = nb2 == 0 ? 2 : 0;
;             const size_t rs = (size_t)64 * dil;
; #pragma unroll
;     ...
;             if (tid < 256) { const int st = tid - 64; tab[tid] = (st >= 0 && st <= 128) ? relb[t5_bucket(st * dil) * 6 + h] : -INFINITY; }
;             const size_t trow = (size_t)(256 * nb2 + 32 * wid + r32) * dil + res;
;             const bf16_t* Q = proj + ((size_t)(16 + h) * NTOK + rb + trow) * 64;
; #pragma unroll
;             for (int d0 = 0; d0 < 4; ++d0) qr[d0] = *(const bf16x8*)(Q + d0 * 16 + hi * 8);
;         } else {
;             const int v2 = u - AT_NFOX - AT_NDIL, qb = 15 - v2 / 48, bh = v2 % 48, b = bh / 6, h = bh % 6, q0 = qb * 256;
;             const size_t rb = (size_t)b * S;
;             const bf16_t* Kb = proj + ((size_t)(40 + h) * NTOK + rb) * 64;
;             const bf16_t* Vb = proj + ((size_t)(46 + h) * NTOK + rb) * 64;
;             const int jhi = (q0 + 254) >> 6;
;             if (!(dbg & 1)) { SB_ISSUE(0); SB_ISSUE(1); SB_ISSUE(2); }
	v_writelane_b32 v252, s19, 58
	v_writelane_b32 v255, s5, 12
	s_and_b64 s[4:5], s[4:5], exec
	s_cselect_b32 s13, s61, s6
	s_cmpk_lt_i32 s13, 0xe00
	s_cselect_b64 s[4:5], -1, 0
	v_writelane_b32 v255, s4, 13
	s_cmpk_gt_i32 s13, 0x1ff
	s_mov_b32 s17, s67
	v_writelane_b32 v255, s5, 14
	s_cselect_b64 s[4:5], -1, 0
	v_writelane_b32 v255, s4, 15
	s_cmpk_gt_u32 s13, 0xaff
	v_writelane_b32 v252, s20, 59
	v_writelane_b32 v255, s5, 16
	s_cselect_b64 s[4:5], -1, 0
	v_writelane_b32 v255, s4, 17
	v_writelane_b32 v252, s21, 60
	s_mov_b32 s21, s67
	v_writelane_b32 v255, s5, 18
	s_add_i32 s4, s13, 0xf500
	s_and_b32 s5, s4, 0xffff
	s_mul_i32 s5, s5, 0xaaab
	s_lshr_b32 s5, s5, 21
	s_mul_i32 s6, s5, 48
	s_sub_i32 s4, s4, s6
	s_and_b32 s6, s4, 0xff
	s_mulk_i32 s6, 0xab
	s_bfe_u32 s6, s6, 0x6000a
	s_mul_i32 s7, s6, 6
	s_sub_i32 s4, s4, s7
	s_and_b32 s4, s4, 0xff
	s_lshl_b32 s6, s6, 12
	s_lshl_b32 s4, s4, 15
	s_add_i32 s7, s6, s4
	s_lshl_b32 s7, s7, 7
	s_add_i32 s8, s7, 0xb800000
	s_add_u32 s8, s96, s8
	s_addc_u32 s9, s97, 0
	s_add_i32 s7, s7, 0xa000000
	s_add_u32 s7, s96, s7
	s_addc_u32 s10, s97, 0
	s_lshl_b32 s11, s5, 14
	s_sub_i32 s12, 0x3f000, s11
	s_lshl_b32 s12, s12, 1
	s_add_u32 s14, s7, s12
	s_addc_u32 s15, s10, 0
	v_writelane_b32 v255, s14, 19
	v_writelane_b32 v252, s22, 61
	v_writelane_b32 v252, s23, 62
	v_writelane_b32 v255, s15, 20
	s_add_u32 s14, s8, s12
	s_addc_u32 s15, s9, 0
	s_sub_i32 s12, 0x3e000, s11
	v_writelane_b32 v255, s14, 21
	s_lshl_b32 s12, s12, 1
	v_writelane_b32 v252, s24, 63
	v_writelane_b32 v255, s15, 22
	s_add_u32 s14, s7, s12
	s_addc_u32 s15, s10, 0
	v_writelane_b32 v255, s14, 23
	s_movk_i32 s56, 0x7f
	s_mov_b32 s57, 0xff800000
	v_writelane_b32 v255, s15, 24
	s_add_u32 s14, s8, s12
	s_addc_u32 s15, s9, 0
	s_sub_i32 s11, 0x3d000, s11
	v_writelane_b32 v255, s14, 25
	s_lshl_b32 s11, s11, 1
	s_mov_b32 s65, 0xc2ce8ed0
	v_writelane_b32 v255, s15, 26
	s_add_u32 s14, s7, s11
	s_addc_u32 s15, s10, 0
	s_add_u32 s8, s8, s11
	s_addc_u32 s9, s9, 0
	s_lshl_b32 s5, s5, 8
	s_sub_i32 s4, s4, s5
	s_add_i32 s5, s13, 0xfe00
	s_add_i32 s4, s4, s6
	s_and_b32 s6, s5, 0xffff
	s_mul_i32 s6, s6, 0xaaab
	s_lshr_b32 s7, s6, 21
	s_mul_i32 s7, s7, 48
	s_sub_i32 s5, s5, s7
	v_writelane_b32 v255, s14, 27
	s_and_b32 s7, s5, 0xff
	s_mulk_i32 s7, 0xab
	v_writelane_b32 v255, s15, 28
	v_writelane_b32 v255, s8, 29
	s_bfe_u32 s7, s7, 0x6000a
	s_add_i32 s4, s4, 0x110f00
	v_writelane_b32 v255, s9, 30
	s_mul_i32 s8, s7, 6
	s_sub_i32 s5, s5, s8
	s_and_b32 s5, s5, 0xff
	s_lshl_b32 s7, s7, 12
	s_lshl_b32 s8, s5, 15
	s_add_i32 s7, s7, s8
	v_writelane_b32 v255, s4, 31
	s_bfe_u32 s4, s6, 0x40015
	s_lshl_b32 s6, s7, 7
	s_add_u32 s6, s96, s6
	s_addc_u32 s8, s97, 0
	s_add_u32 s9, s6, 0x5800000
	s_addc_u32 s10, s8, 0
	s_add_u32 s6, s6, 0x7000000
	s_addc_u32 s8, s8, 0
	s_lshl_b32 s11, s4, 7
	s_or_b32 s12, s11, 0x60000
	s_add_u32 s14, s9, s12
	s_addc_u32 s15, s10, 0
	v_writelane_b32 v255, s14, 32
	s_mov_b64 s[44:45], -1
	s_mov_b64 s[86:87], 0x800
	v_writelane_b32 v255, s15, 33
	s_add_u32 s14, s6, s12
	s_addc_u32 s15, s8, 0
	v_writelane_b32 v255, s14, 34
	s_or_b32 s12, s11, 0x40000
	s_mov_b32 s60, 0xbfb8aa3b
	v_writelane_b32 v255, s15, 35
	s_add_u32 s14, s9, s12
	s_addc_u32 s15, s10, 0
	v_writelane_b32 v255, s14, 36
	s_mov_b64 s[88:89], 0x80
	s_mov_b64 s[94:95], 0x100
	v_writelane_b32 v255, s15, 37
	s_add_u32 s14, s6, s12
	s_addc_u32 s15, s8, 0
	v_writelane_b32 v255, s14, 38
	s_or_b32 s12, s11, 0x20000
	s_mov_b32 s62, s67
	v_writelane_b32 v255, s15, 39
	s_add_u32 s14, s9, s12
	s_addc_u32 s15, s10, 0
	v_writelane_b32 v255, s14, 40
	s_nop 1
	v_writelane_b32 v255, s15, 41
	s_add_u32 s14, s6, s12
	s_addc_u32 s15, s8, 0
	v_writelane_b32 v255, s14, 42
	s_nop 1
	v_writelane_b32 v255, s15, 43
	s_add_u32 s14, s9, s11
	s_addc_u32 s15, s10, 0
	v_writelane_b32 v255, s14, 44
	s_add_u32 s10, s6, s11
	s_addc_u32 s11, s8, 0
	v_writelane_b32 v255, s15, 45
	s_lshl_b32 s5, s5, 2
	v_writelane_b32 v255, s10, 46
	s_add_i32 s5, s5, 0
	s_add_i32 s5, s5, 0x21f00
	v_writelane_b32 v255, s11, 47
	v_writelane_b32 v255, s5, 48
	s_ashr_i32 s5, s13, 5
	s_or_b32 s4, s7, s4
	s_sub_i32 s5, 15, s5
	s_lshl_b32 s6, s13, 10
	s_and_b32 s7, s13, 31
	s_and_b32 s6, s6, 0x7000
	s_lshl_b32 s7, s7, 14
	s_or_b32 s14, s4, 0x80000
	s_and_b32 s8, s13, 3
	s_lshl_b32 s16, s5, 8
	s_add_u32 s18, s28, s7
	s_addc_u32 s19, s29, 0
	s_lshl_b32 s7, s5, 2
	v_writelane_b32 v255, s13, 49
	s_or_b32 s20, s7, 3
	s_lshl_b64 s[4:5], s[16:17], 2
	v_writelane_b32 v255, s28, 50
	s_add_u32 s4, s18, s4
	v_writelane_b32 v255, s29, 51
	s_addc_u32 s5, s19, s5
	v_writelane_b32 v255, s4, 52
	s_mov_b32 s15, s67
	s_nop 0
	v_writelane_b32 v255, s5, 53
	s_lshl_b32 s4, s8, 22
	s_lshl_b32 s5, s6, 7
	s_or_b32 s4, s5, s4
	s_add_u32 s4, s96, s4
	s_addc_u32 s5, s97, 0
	s_add_u32 s9, s4, 0x2000000
	s_addc_u32 s10, s5, 0
	s_add_u32 s11, s4, 0x1000000
	s_addc_u32 s12, s5, 0
	s_lshl_b64 s[4:5], s[20:21], 13
	s_add_u32 s22, s11, s4
	s_addc_u32 s23, s12, s5
	v_writelane_b32 v255, s22, 54
	s_add_u32 s4, s9, s4
	s_addc_u32 s5, s10, s5
	v_writelane_b32 v255, s23, 55
	v_writelane_b32 v255, s4, 56
	s_lshl_b32 s66, s20, 6
	s_nop 0
	v_writelane_b32 v255, s5, 57
	s_mov_b32 s4, s20
	v_writelane_b32 v255, s4, 58
	s_nop 1
	v_writelane_b32 v255, s5, 59
	s_lshl_b64 s[4:5], s[66:67], 2
	s_add_u32 s4, s18, s4
	s_addc_u32 s5, s19, s5
; #define LAS __attribute__((address_space(3)))
; #define FOX_ISSUE(i) do { const int j_ = jhi - (i), bf_ = (i) & 3; dma_kv(lds, bf_, Kb + (size_t)j_ * 4096, Vb + (size_t)j_ * 4096, 64, wid, lane); \
;         glds4(cum + j_ * 64 + lane, (unsigned)__builtin_amdgcn_readfirstlane(l0 + L_CK + bf_ * 256)); } while (0)
;     ...
;     bf16x8 qr[4];
;     float fox_cr = 0.f, fox_cv = 0.f, fox_cq = 0.f;
;     auto prologue = [&](int u) {
;         if (!UNIT_ON(u)) return;
;         int lane = tid & 63; asm volatile("" : "+v"(lane));
;         const int r32 = lane & 31, hi = lane >> 5;
;         if (u < AT_NFOX) {
;             const int qb = 15 - (u >> 5), bh = u & 31, b = bh >> 2, h = bh & 3, q0 = qb * 256;
;             const size_t rb = (size_t)b * S;
;             const bf16_t* Kb = proj + ((size_t)(4 + h) * NTOK + rb) * 64;
;             const bf16_t* Vb = proj + ((size_t)(8 + h) * NTOK + rb) * 64;
;             const float* cum = cumall + (size_t)bh * S;
;             const int jhi = 4 * qb + 3;
;             fox_cr = cum[q0]; fox_cv = cum[64 * (lane <= jhi ? lane : jhi) + 63]; fox_cq = cum[q0 + 32 * wid + r32];
;             if (!(dbg & 1)) { FOX_ISSUE(0); FOX_ISSUE(1); FOX_ISSUE(2); }
;             const bf16_t* Q = proj + ((size_t)(0 + h) * NTOK + rb + q0 + 32 * wid + r32) * 64;
; #pragma unroll
;             for (int d0 = 0; d0 < 4; ++d0) qr[d0] = *(const bf16x8*)(Q + d0 * 16 + hi * 8);
; __device__ __forceinline__ void op_mfma(const Args& a, LAS unsigned char* lds, int layer, bf16_t* outp = nullptr) {
;     pg8::DenseOrder So; So.init(a.ws + WS_ACT, a.ws + WS_WOUT + (size_t)layer * D * D * 2, NTOK, D, D, gridDim.x, blockIdx.x, (size_t)256 * 128);
;     bf16_t* xb = (bf16_t*)(a.ws + WS_XB);
;     EpiOut E{layer == 0 ? a.in[I_X] : nullptr, xb, outp ? outp : xb, (const float*)(a.ws + WS_MOD) + (size_t)layer * NB * 6144 + 2048};
;     pg8::gemm_phase<EpiOut, pg8::DenseOrder>(lds, D, So, E, 128u, (size_t)NTOK * 128);
	v_writelane_b32 v255, s4, 60
	s_or_b32 s66, s7, 2
	s_nop 0
	v_writelane_b32 v255, s5, 61
	s_lshl_b64 s[4:5], s[66:67], 13
	s_add_u32 s20, s11, s4
	s_addc_u32 s21, s12, s5
	s_add_u32 s4, s9, s4
	s_addc_u32 s5, s10, s5
	v_writelane_b32 v253, s4, 0
	s_lshl_b32 s66, s66, 6
	v_writelane_b32 v255, s20, 62
	v_writelane_b32 v253, s5, 1
	s_lshl_b64 s[4:5], s[66:67], 2
	s_add_u32 s4, s18, s4
	s_addc_u32 s5, s19, s5
	v_writelane_b32 v253, s4, 2
	s_or_b32 s66, s7, 1
	v_writelane_b32 v255, s21, 63
	v_writelane_b32 v253, s5, 3
	s_lshl_b64 s[4:5], s[66:67], 13
	s_add_u32 s20, s11, s4
	s_addc_u32 s21, s12, s5
	v_writelane_b32 v253, s20, 4
	s_add_u32 s4, s9, s4
	s_addc_u32 s5, s10, s5
	v_writelane_b32 v253, s21, 5
	v_writelane_b32 v253, s4, 6
	s_lshl_b32 s66, s66, 6
	s_mov_b32 s9, s67
	v_writelane_b32 v253, s5, 7
	s_lshl_b64 s[4:5], s[66:67], 2
	s_add_u32 s4, s18, s4
	v_writelane_b32 v253, s18, 8
	s_addc_u32 s5, s19, s5
	s_nop 0
	v_writelane_b32 v253, s19, 9
	v_writelane_b32 v253, s4, 10
	s_nop 1
	v_writelane_b32 v253, s5, 11
	s_lshl_b32 s4, s8, 15
	s_or_b32 s4, s6, s4
	s_mov_b32 s6, s16
	v_writelane_b32 v253, s6, 12
	s_add_i32 s4, s4, s16
	s_mov_b32 s8, s77
	v_writelane_b32 v253, s7, 13
	s_mov_b32 s6, s61
	s_mov_b32 s7, s67
	v_writelane_b32 v253, s4, 14
	s_lshl_b64 s[4:5], s[6:7], 9
	s_lshl_b64 s[70:71], s[8:9], 9
	v_writelane_b32 v253, s4, 15
	s_nop 1
	v_writelane_b32 v253, s5, 16
	s_add_u32 s4, s92, 0x8c00000
	s_addc_u32 s5, s93, 0
	v_writelane_b32 v253, s4, 17
	s_nop 1
	v_writelane_b32 v253, s5, 18
	s_add_u32 s4, s92, 0x1700000
	v_writelane_b32 v253, s4, 19
	s_addc_u32 s4, s93, 0
	v_writelane_b32 v253, s4, 20
	s_add_u32 s4, s92, 0x10000
	v_writelane_b32 v253, s4, 21
	s_addc_u32 s4, s93, 0
	v_writelane_b32 v253, s4, 22
	s_add_u32 s4, s92, 0x300000
	s_addc_u32 s5, s93, 0
	v_writelane_b32 v253, s4, 23
	s_nop 1
	v_writelane_b32 v253, s5, 24
	s_add_u32 s4, s92, 0x500000
	s_addc_u32 s5, s93, 0
	v_writelane_b32 v253, s4, 25
	s_cmpk_lt_i32 s61, 0x100
	s_nop 0
	v_writelane_b32 v253, s5, 26
	s_cselect_b64 s[4:5], -1, 0
	v_writelane_b32 v253, s4, 27
	s_nop 1
	v_writelane_b32 v253, s5, 28
	s_add_u32 s4, s92, 0x14400000
	s_addc_u32 s5, s93, 0
	v_writelane_b32 v253, s4, 29
	s_nop 1
	v_writelane_b32 v253, s5, 30
	s_add_i32 s4, s77, s61
	v_writelane_b32 v253, s4, 31
	s_add_u32 s4, s92, 0x7c00080
	s_addc_u32 s5, s93, 0
	s_add_i32 s2, s3, s2
	s_ashr_i32 s3, s2, 31
	s_lshr_b32 s3, s3, 27
	v_writelane_b32 v253, s4, 32
	s_add_i32 s3, s2, s3
	s_nop 0
	v_writelane_b32 v253, s5, 33
	s_and_b32 s4, s3, 0xffe0
	s_sub_i32 s2, s2, s4
	s_bfe_i32 s4, s2, 0x80000
	s_bfe_u32 s4, s4, 0x3000c
	s_add_i32 s4, s2, s4
	s_and_b32 s5, s4, 0xf8
	s_sub_i32 s2, s2, s5
	s_ashr_i32 s3, s3, 5
	s_bfe_i32 s4, s4, 0x80000
	s_lshl_b32 s3, s3, 3
	s_sext_i32_i16 s4, s4
	s_sext_i32_i8 s2, s2
	s_add_i32 s10, s3, s2
	s_ashr_i32 s2, s4, 3
	v_writelane_b32 v253, s2, 34
	s_lshr_b32 s2, s4, 3
	s_mov_b32 s4, s10
	s_ashr_i32 s11, s10, 31
	v_writelane_b32 v253, s4, 35
	s_nop 1
	v_writelane_b32 v253, s5, 36
	s_lshl_b64 s[4:5], s[10:11], 15
	s_add_u32 s4, s80, s4
	s_addc_u32 s5, s81, s5
	v_writelane_b32 v253, s14, 37
	s_bfe_i64 s[2:3], s[2:3], 0x100000
	s_lshl_b64 s[2:3], s[2:3], 19
	v_writelane_b32 v253, s15, 38
	v_writelane_b32 v253, s2, 39
	s_nop 1
	v_writelane_b32 v253, s3, 40
	s_add_u32 s2, s4, 0x4000
	s_addc_u32 s3, s5, 0
	v_writelane_b32 v253, s2, 41
	s_nop 1
	v_writelane_b32 v253, s3, 42
	s_add_u32 s2, s4, 0x400000
	v_writelane_b32 v253, s4, 43
	s_addc_u32 s3, s5, 0
	s_lshl_b64 s[52:53], s[8:9], 10
	v_writelane_b32 v253, s5, 44
	v_writelane_b32 v253, s2, 45
	s_add_i32 s64, 0, 0x13000
	s_nop 0
	v_writelane_b32 v253, s3, 46
	s_lshl_b32 s2, s61, 7
	v_writelane_b32 v253, s2, 47
	s_lshl_b32 s2, s77, 7
	v_writelane_b32 v253, s2, 48
	s_mul_i32 s2, s77, 0x3000
	v_writelane_b32 v253, s2, 49
	s_add_i32 s2, 0, 0x21c20
	v_writelane_b32 v253, s2, 50
	s_add_i32 s2, 0, 0x21c24
	v_writelane_b32 v253, s2, 51
	s_add_i32 s2, 0, 0x21000
	v_writelane_b32 v253, s2, 52
	s_add_i32 s2, 0, 0x21100
	v_writelane_b32 v253, s2, 53
	s_add_i32 s2, 0, 0x21200
	v_writelane_b32 v253, s2, 54
	s_add_i32 s2, 0, 0x21504
	v_writelane_b32 v253, s2, 55
	s_add_i32 s2, 0, 0x15040
	v_writelane_b32 v253, s2, 56
	s_add_i32 s2, 0, 0x15000
	v_writelane_b32 v253, s2, 57
	s_add_i32 s2, 0, 0x21e80
	v_writelane_b32 v253, s2, 58
	s_add_i32 s2, 0, 0x21e10
	v_writelane_b32 v253, s2, 59
	s_add_i32 s2, 0, 0x21e20
	v_writelane_b32 v253, s2, 60
	s_add_i32 s2, 0, 0x21e30
	v_writelane_b32 v253, s2, 61
	v_writelane_b32 v253, s54, 62
	s_load_dwordx2 s[4:5], s[54:55], 0x0
	s_mov_b32 s3, 0x42b17218
	v_writelane_b32 v253, s55, 63
	s_waitcnt lgkmcnt(0)
	v_writelane_b32 v254, s4, 0
	s_nop 1
	v_writelane_b32 v254, s5, 1
	s_lshl_b64 s[4:5], s[8:9], 13
	v_writelane_b32 v254, s4, 2
	s_nop 1
	v_writelane_b32 v254, s5, 3
	v_writelane_b32 v254, s6, 4
	s_lshl_b64 s[4:5], s[6:7], 12
	s_nop 0
	v_writelane_b32 v254, s7, 5
	v_writelane_b32 v254, s4, 6
	s_nop 1
	v_writelane_b32 v254, s5, 7
	s_lshl_b64 s[4:5], s[8:9], 14
	v_writelane_b32 v254, s4, 8
	s_nop 1
	v_writelane_b32 v254, s5, 9
	v_writelane_b32 v254, s8, 10
	s_lshl_b64 s[4:5], s[8:9], 12
	s_nop 0
	v_writelane_b32 v254, s9, 11
	v_writelane_b32 v254, s4, 12
	s_nop 1
	v_writelane_b32 v254, s5, 13
	v_writelane_b32 v254, s82, 14
	s_nop 1
	v_writelane_b32 v254, s83, 15
	s_branch .LBB0_104

; #define LAS __attribute__((address_space(3)))
; __device__ __forceinline__ int opaque_tid() { int t = threadIdx.x; asm volatile("" : "+v"(t)); return t; }
;     const int tid = opaque_tid(), lane = tid & 63, wave = tid >> 6;
;     LAS float* scr = (LAS float*)(lds + 49152) + wave * (64 * 33);
;     const int gw = ((int)blockIdx.x - blk0) * NWAVES + wave, ngw = nblk * NWAVES;
;     constexpr int I_L = 16 * 104 + 16 * 32 + 16 * 16 * 32 + 16 * 8 * 32;
;     if ((int)blockIdx.x < blk0 || (int)blockIdx.x >= blk0 + nblk) return;
;     float tv[32];
;     const int I_E = it_hi < I_L ? it_hi : I_L;
;     int it = it_lo + gw;
; __device__ __forceinline__ void pj_mfma(const Args& a, LAS unsigned char* lds, int layer) {
;     ...
;     if (layer + 1 < NL) { __syncthreads(); constexpr int I_SPLIT = 10240;
;         const int half = gridDim.x / 2; const bool upper = (int)blockIdx.x >= half;
;         p0_prep(a, lds, layer + 1, upper ? half : 0, upper ? (int)gridDim.x - half : half, upper ? 0 : I_SPLIT, upper ? I_SPLIT : (1 << 30)); }
.Lpj_l1_prep:
	s_lshr_b32 s4, s77, 1
	s_sub_i32 s5, s77, s4
	s_cmp_ge_u32 s61, s4
	s_cselect_b64 s[6:7], -1, 0
	s_sub_i32 s8, s61, s4
	s_lshl_b32 s8, s8, 3
	s_addk_i32 s8, 0x1570
	s_lshl_b32 s5, s5, 3
	s_movk_i32 s9, 0x2880
	s_nop 0
	v_writelane_b32 v252, s9, 36
	v_writelane_b32 v252, s5, 37
	v_writelane_b32 v252, s6, 38
	v_writelane_b32 v252, s7, 39
	v_writelane_b32 v252, s8, 40
	s_branch .Lprep_go
